# k_sort: all output stores written through (sc1); its results are only read on other XCDs
# speedup vs baseline: 1.0151x; 1.0020x over previous
_Z6k_sortPKfS0_PKiS2_PiP15HIP_vector_typeIfLj4EEPfS7_S3_S7_S7_S3_S3_S6_S6_:
	s_load_dwordx2 s[4:5], s[0:1], 0x70
	s_load_dwordx8 s[8:15], s[0:1], 0x0
	s_load_dwordx8 s[36:43], s[0:1], 0x40
	s_load_dwordx2 s[44:45], s[0:1], 0x60
	s_load_dwordx2 s[46:47], s[0:1], 0x20
	s_load_dwordx4 s[48:51], s[0:1], 0x30
	s_mov_b32 s17, 0
	s_mov_b32 s16, s17
	v_lshl_or_b32 v2, s2, 12, v0
	v_mov_b32_e32 v3, 0
	s_mov_b32 s18, s17
	s_mov_b32 s19, s17
	v_mov_b64_e32 v[6:7], s[16:17]
	s_waitcnt lgkmcnt(0)
	v_lshl_add_u64 v[4:5], v[2:3], 4, s[4:5]
	v_mov_b64_e32 v[8:9], s[18:19]
	global_store_dwordx4 v[4:5], v[6:9], off sc1
	v_or_b32_e32 v4, 0x400, v2
	v_mov_b32_e32 v5, v3
	v_lshl_add_u64 v[4:5], v[4:5], 4, s[4:5]
	global_store_dwordx4 v[4:5], v[6:9], off sc1
	v_or_b32_e32 v4, 0x800, v2
	v_mov_b32_e32 v5, v3
	v_lshl_add_u64 v[4:5], v[4:5], 4, s[4:5]
	v_or_b32_e32 v2, 0xc00, v2
	s_movk_i32 s3, 0x100
	global_store_dwordx4 v[4:5], v[6:9], off sc1
	v_lshl_add_u64 v[4:5], v[2:3], 4, s[4:5]
	v_cmp_gt_u32_e64 s[6:7], s3, v0
	global_store_dwordx4 v[4:5], v[6:9], off sc1
	s_and_saveexec_b64 s[4:5], s[6:7]
	v_mov_b32_e32 v1, 0x10400
	v_lshl_add_u32 v1, v0, 2, v1
	ds_write_b32 v1, v3
	s_or_b64 exec, exec, s[4:5]
	s_lshr_b32 s28, s2, 1
	s_and_b32 s18, s2, 1
	s_bitcmp1_b32 s2, 0
	s_cselect_b64 s[2:3], -1, 0
	s_lshl_b32 s16, s28, 12
	s_lshl_b64 s[4:5], s[16:17], 3
	s_cmp_eq_u32 s18, 0
	s_cselect_b32 s8, s8, s10
	s_cselect_b32 s9, s9, s11
	s_cselect_b32 s10, s12, s14
	s_cselect_b32 s11, s13, s15
	s_add_u32 s4, s8, s4
	v_or_b32_e32 v13, 0x400, v0
	s_addc_u32 s5, s9, s5
	v_lshlrev_b32_e32 v1, 3, v0
	v_lshlrev_b32_e32 v2, 3, v13
	v_or_b32_e32 v12, 0x800, v0
	global_load_dwordx2 v[8:9], v1, s[4:5]
	global_load_dwordx2 v[4:5], v2, s[4:5]
	v_lshlrev_b32_e32 v2, 3, v12
	v_or_b32_e32 v10, 0xc00, v0
	global_load_dwordx2 v[6:7], v2, s[4:5]
	v_lshlrev_b32_e32 v2, 3, v10
	global_load_dwordx2 v[2:3], v2, s[4:5]
	s_lshl_b64 s[4:5], s[16:17], 2
	s_add_u32 s4, s10, s4
	s_addc_u32 s5, s11, s5
	v_lshlrev_b32_e32 v11, 2, v0
	v_lshlrev_b32_e32 v14, 2, v13
	global_load_dword v17, v11, s[4:5]
	global_load_dword v16, v14, s[4:5]
	v_lshlrev_b32_e32 v14, 2, v12
	global_load_dword v15, v14, s[4:5]
	v_lshlrev_b32_e32 v14, 2, v10
	global_load_dword v14, v14, s[4:5]
	v_mov_b32_e32 v20, 0
	ds_write2st64_b32 v11, v20, v20 offset0:192 offset1:208
	ds_write2st64_b32 v11, v20, v20 offset0:224 offset1:240
	v_mov_b32_e32 v18, 0xff
	v_mov_b32_e32 v25, 0x10400
	v_mov_b32_e32 v19, 1
	s_waitcnt lgkmcnt(0)
	s_barrier
	v_cmp_gt_u32_e32 vcc, 64, v0
	s_waitcnt vmcnt(7)
	v_mul_f32_e32 v20, 0x43800000, v8
	s_waitcnt vmcnt(6)
	v_mul_f32_e32 v21, 0x43800000, v4
	v_cvt_i32_f32_e32 v20, v20
	v_cvt_i32_f32_e32 v21, v21
	s_waitcnt vmcnt(5)
	v_mul_f32_e32 v22, 0x43800000, v6
	v_cvt_i32_f32_e32 v22, v22
	s_waitcnt vmcnt(4)
	v_mul_f32_e32 v23, 0x43800000, v2
	v_cvt_i32_f32_e32 v23, v23
	v_med3_i32 v26, v20, 0, v18
	v_med3_i32 v20, v21, 0, v18
	v_med3_i32 v22, v22, 0, v18
	v_med3_i32 v24, v23, 0, v18
	v_lshl_add_u32 v21, v26, 2, v25
	v_lshl_add_u32 v23, v20, 2, v25
	v_lshl_add_u32 v28, v22, 2, v25
	ds_add_rtn_u32 v27, v21, v19
	ds_add_rtn_u32 v21, v23, v19
	ds_add_rtn_u32 v23, v28, v19
	v_lshl_add_u32 v25, v24, 2, v25
	ds_add_rtn_u32 v25, v25, v19
	s_waitcnt lgkmcnt(0)
	s_barrier
	s_and_saveexec_b64 s[4:5], vcc
	s_cbranch_execz .LBB0_4
	v_lshlrev_b32_e32 v33, 4, v0
	v_add_u32_e32 v28, 0x10400, v33
	ds_read_b128 v[28:31], v28
	v_mov_b32_e32 v32, 0
	s_waitcnt lgkmcnt(0)
	v_add_u32_e32 v34, v29, v28
	v_add3_u32 v31, v34, v30, v31
	s_nop 1
	v_add_u32_dpp v34, v31, v31 row_shr:1 row_mask:0xf bank_mask:0xf bound_ctrl:1
	s_nop 1
	v_add_u32_dpp v34, v34, v34 row_shr:2 row_mask:0xf bank_mask:0xf bound_ctrl:1
	s_nop 1
	v_add_u32_dpp v34, v34, v34 row_shr:4 row_mask:0xf bank_mask:0xf bound_ctrl:1
	s_nop 1
	v_add_u32_dpp v34, v34, v34 row_shr:8 row_mask:0xf bank_mask:0xf bound_ctrl:1
	s_nop 1
	v_add_u32_dpp v34, v34, v34 row_bcast:15 row_mask:0xa bank_mask:0xf
	s_nop 1
	v_mov_b32_dpp v32, v34 row_bcast:31 row_mask:0xc bank_mask:0xf
	v_sub_u32_e32 v31, v32, v31
	v_add_u32_e32 v32, v31, v34
	v_or_b32_e32 v31, 0x10000, v33
	v_add_u32_e32 v33, v32, v28
	v_add_u32_e32 v34, v33, v29
	v_add_u32_e32 v35, v34, v30
	ds_write_b128 v31, v[32:35]

.LBB0_6:
	s_or_b64 exec, exec, s[4:5]
	s_waitcnt lgkmcnt(0)
	s_barrier
	ds_read_b32 v19, v29
	v_lshl_add_u32 v26, v26, s8, v27
	ds_read_b32 v27, v30
	ds_read_b32 v28, v28
	ds_read_b32 v25, v25
	s_waitcnt vmcnt(3)
	v_cmp_eq_u32_e32 vcc, 0, v17
	s_mov_b64 s[4:5], -1
	s_waitcnt lgkmcnt(3)
	v_add_lshl_u32 v19, v26, v19, 2
	ds_write2st64_b32 v19, v8, v9 offset1:64
	v_bfrev_b32_e32 v8, 1
	v_cndmask_b32_e32 v8, 0, v8, vcc
	v_or_b32_e32 v8, v8, v0
	ds_write_b32 v19, v8 offset:32768
	v_lshl_add_u32 v8, v20, s8, v21
	s_waitcnt lgkmcnt(4)
	v_add_lshl_u32 v8, v8, v27, 2
	ds_write2st64_b32 v8, v4, v5 offset1:64
	v_mov_b32_e32 v4, 0x400
	v_mov_b32_e32 v5, 0x80000400
	s_waitcnt vmcnt(2)
	v_cmp_eq_u32_e32 vcc, 0, v16
	s_nop 1
	v_cndmask_b32_e32 v4, v4, v5, vcc
	v_or_b32_e32 v4, v4, v0
	ds_write_b32 v8, v4 offset:32768
	v_lshl_add_u32 v4, v22, s8, v23
	s_waitcnt lgkmcnt(5)
	v_add_lshl_u32 v4, v4, v28, 2
	ds_write2st64_b32 v4, v6, v7 offset1:64
	v_mov_b32_e32 v5, 0x800
	v_mov_b32_e32 v6, 0x80000800
	s_waitcnt vmcnt(1)
	v_cmp_eq_u32_e32 vcc, 0, v15
	s_nop 1
	v_cndmask_b32_e32 v5, v5, v6, vcc
	v_or_b32_e32 v5, v5, v0
	ds_write_b32 v4, v5 offset:32768
	v_lshl_add_u32 v4, v24, s8, v18
	s_waitcnt lgkmcnt(6)
	v_add_lshl_u32 v4, v4, v25, 2
	ds_write2st64_b32 v4, v2, v3 offset1:64
	v_mov_b32_e32 v2, 0xc00
	v_mov_b32_e32 v3, 0x80000c00
	s_waitcnt vmcnt(0)
	v_cmp_eq_u32_e32 vcc, 0, v14
	s_nop 1
	v_cndmask_b32_e32 v2, v2, v3, vcc
	v_or_b32_e32 v2, v2, v0
	ds_write_b32 v4, v2 offset:32768
	s_waitcnt lgkmcnt(0)
	s_barrier
	s_getpc_b64 s[30:31]
	s_add_u32 s30, s30, 0x24b8
	s_addc_u32 s31, s31, 0
	v_lshlrev_b32_e32 v40, 6, v0
	v_min_u32_e32 v40, 0x2f00, v40
	global_load_dword v40, v40, s[30:31]
	s_and_b32 s32, s0, 0xfffff000
	s_mov_b32 s33, s1
	v_and_b32_e32 v41, 63, v0
	v_lshlrev_b32_e32 v41, 6, v41
	global_load_dword v41, v41, s[32:33]
	ds_read_b32 v14, v11 offset:32768
	s_mov_b64 s[18:19], s[44:45]
	s_mov_b64 s[8:9], s[36:37]
	s_mov_b64 s[10:11], s[38:39]
	s_mov_b64 s[12:13], s[40:41]
	s_mov_b64 s[14:15], s[42:43]
	ds_read2st64_b32 v[4:5], v11 offset1:64
	v_or_b32_e32 v2, s16, v0
	v_mov_b32_e32 v3, 0
	s_waitcnt lgkmcnt(0)
	v_and_b32_e32 v15, 0x7fffffff, v14
	s_and_b64 vcc, exec, s[2:3]
	v_lshlrev_b64 v[6:7], 2, v[2:3]
	s_cbranch_vccz .LBB0_8
	v_lshl_add_u64 v[8:9], s[10:11], 0, v[6:7]
	global_store_dword v[8:9], v4, off sc1
	v_lshl_add_u64 v[8:9], s[12:13], 0, v[6:7]
	global_store_dword v[8:9], v5, off sc1
	v_lshl_add_u64 v[8:9], s[14:15], 0, v[6:7]
	global_store_dword v[8:9], v15, off sc1
	s_mov_b64 s[4:5], 0
.LBB0_8:
	s_mov_b64 s[24:25], s[46:47]
	s_mov_b64 s[20:21], s[48:49]
	s_mov_b64 s[22:23], s[50:51]
	v_or_b32_e32 v8, 0x4000, v11
	v_or_b32_e32 v9, 0x8000, v11
	s_andn2_b64 vcc, exec, s[4:5]
	s_mov_b64 s[4:5], s[18:19]
	s_cbranch_vccnz .LBB0_10
	s_waitcnt lgkmcnt(0)
	v_lshl_add_u64 v[16:17], s[24:25], 0, v[6:7]
	global_store_dword v[16:17], v15, off sc1
	v_lshl_add_u64 v[16:17], s[20:21], 0, v[6:7]
	v_lshl_add_u64 v[6:7], s[22:23], 0, v[6:7]
	s_mov_b64 s[4:5], s[8:9]
	global_store_dword v[16:17], v4, off sc1
	global_store_dword v[6:7], v5, off sc1
.LBB0_10:
	ds_read_b32 v15, v11 offset:4096
	ds_read_b32 v7, v8 offset:4096
	ds_read_b32 v6, v9 offset:4096
	v_not_b32_e32 v4, v14
	v_lshrrev_b32_e32 v4, 31, v4
	v_lshl_add_u64 v[2:3], v[2:3], 2, s[4:5]
	global_store_dword v[2:3], v4, off sc1
	v_or_b32_e32 v2, s16, v13
	v_mov_b32_e32 v3, 0
	v_cndmask_b32_e64 v4, 0, 1, s[2:3]
	s_waitcnt lgkmcnt(0)
	v_and_b32_e32 v14, 0x7fffffff, v6
	s_mov_b64 s[26:27], -1
	v_cmp_ne_u32_e64 s[4:5], 1, v4
	s_andn2_b64 vcc, exec, s[2:3]
	v_lshlrev_b64 v[4:5], 2, v[2:3]
	s_cbranch_vccnz .LBB0_12
	v_lshl_add_u64 v[16:17], s[10:11], 0, v[4:5]
	global_store_dword v[16:17], v15, off sc1
	v_lshl_add_u64 v[16:17], s[12:13], 0, v[4:5]
	global_store_dword v[16:17], v7, off sc1
	v_lshl_add_u64 v[16:17], s[14:15], 0, v[4:5]
	s_mov_b64 s[26:27], 0
	global_store_dword v[16:17], v14, off sc1
.LBB0_12:
	s_andn2_b64 vcc, exec, s[26:27]
	s_mov_b64 s[26:27], s[18:19]
	s_cbranch_vccnz .LBB0_14
	v_lshl_add_u64 v[16:17], s[24:25], 0, v[4:5]
	global_store_dword v[16:17], v14, off sc1
	v_lshl_add_u64 v[16:17], s[20:21], 0, v[4:5]
	v_lshl_add_u64 v[4:5], s[22:23], 0, v[4:5]
	s_mov_b64 s[26:27], s[8:9]
	global_store_dword v[16:17], v15, off sc1
	global_store_dword v[4:5], v7, off sc1
.LBB0_14:
	ds_read_b32 v14, v11 offset:8192
	ds_read_b32 v13, v8 offset:8192
	ds_read_b32 v7, v9 offset:8192
	v_not_b32_e32 v4, v6
	v_lshrrev_b32_e32 v4, 31, v4
	v_lshl_add_u64 v[2:3], v[2:3], 2, s[26:27]
	global_store_dword v[2:3], v4, off sc1
	v_or_b32_e32 v2, s16, v12
	v_mov_b32_e32 v3, 0
	s_waitcnt lgkmcnt(0)
	v_and_b32_e32 v6, 0x7fffffff, v7
	s_mov_b64 s[26:27], -1
	s_and_b64 vcc, exec, s[4:5]
	v_lshlrev_b64 v[4:5], 2, v[2:3]
	s_cbranch_vccnz .LBB0_16
	v_lshl_add_u64 v[16:17], s[10:11], 0, v[4:5]
	global_store_dword v[16:17], v14, off sc1
	v_lshl_add_u64 v[16:17], s[12:13], 0, v[4:5]
	global_store_dword v[16:17], v13, off sc1
	v_lshl_add_u64 v[16:17], s[14:15], 0, v[4:5]
	s_mov_b64 s[26:27], 0
	global_store_dword v[16:17], v6, off sc1
.LBB0_16:
	s_andn2_b64 vcc, exec, s[26:27]
	s_mov_b64 s[26:27], s[18:19]
	s_cbranch_vccnz .LBB0_18
	v_lshl_add_u64 v[16:17], s[24:25], 0, v[4:5]
	global_store_dword v[16:17], v6, off sc1
	v_lshl_add_u64 v[16:17], s[20:21], 0, v[4:5]
	v_lshl_add_u64 v[4:5], s[22:23], 0, v[4:5]
	s_mov_b64 s[26:27], s[8:9]
	global_store_dword v[16:17], v14, off sc1
	global_store_dword v[4:5], v13, off sc1
.LBB0_18:
	ds_read_b32 v11, v11 offset:12288
	ds_read_b32 v8, v8 offset:12288
	ds_read_b32 v6, v9 offset:12288
	v_not_b32_e32 v4, v7
	v_lshrrev_b32_e32 v4, 31, v4
	v_lshl_add_u64 v[2:3], v[2:3], 2, s[26:27]
	global_store_dword v[2:3], v4, off sc1
	v_or_b32_e32 v2, s16, v10
	v_mov_b32_e32 v3, 0
	s_waitcnt lgkmcnt(0)
	v_and_b32_e32 v7, 0x7fffffff, v6
	s_mov_b64 s[16:17], -1
	s_and_b64 vcc, exec, s[4:5]
	v_lshlrev_b64 v[4:5], 2, v[2:3]
	s_cbranch_vccnz .LBB0_20
	v_lshl_add_u64 v[12:13], s[10:11], 0, v[4:5]
	global_store_dword v[12:13], v11, off sc1
	v_lshl_add_u64 v[12:13], s[12:13], 0, v[4:5]
	global_store_dword v[12:13], v8, off sc1
	v_lshl_add_u64 v[12:13], s[14:15], 0, v[4:5]
	s_mov_b64 s[16:17], 0
	global_store_dword v[12:13], v7, off sc1
.LBB0_20:
	s_andn2_b64 vcc, exec, s[16:17]
	s_cbranch_vccnz .LBB0_22
	v_lshl_add_u64 v[12:13], s[24:25], 0, v[4:5]
	global_store_dword v[12:13], v7, off sc1
	v_lshl_add_u64 v[12:13], s[20:21], 0, v[4:5]
	v_lshl_add_u64 v[4:5], s[22:23], 0, v[4:5]
	s_mov_b64 s[18:19], s[8:9]
	global_store_dword v[12:13], v11, off sc1
	global_store_dword v[4:5], v8, off sc1
.LBB0_22:
	s_load_dwordx2 s[4:5], s[0:1], 0x68
	v_not_b32_e32 v4, v6
	v_lshrrev_b32_e32 v4, 31, v4
	v_lshl_add_u64 v[2:3], v[2:3], 2, s[18:19]
	s_and_b64 vcc, exec, s[2:3]
	global_store_dword v[2:3], v4, off sc1
	s_cbranch_vccz .LBB0_28
	s_mov_b64 s[2:3], 0
	s_mov_b64 s[10:11], 0
	s_and_saveexec_b64 s[8:9], s[6:7]
	s_cbranch_execz .LBB0_27
	v_lshlrev_b32_e32 v10, 4, v0
	v_and_b32_e32 v11, 15, v0
	v_add_u32_e32 v4, 1, v0
	v_or_b32_e32 v2, v11, v10
	v_and_or_b32 v4, v4, 15, v10
	v_add_u32_e32 v6, 2, v0
	v_add_u32_e32 v8, 3, v0
	v_lshlrev_b32_e32 v2, 2, v2
	v_lshlrev_b32_e32 v4, 2, v4
	v_and_or_b32 v6, v6, 15, v10
	v_and_or_b32 v8, v8, 15, v10
	ds_read2st64_b32 v[2:3], v2 offset1:64
	ds_read2st64_b32 v[4:5], v4 offset1:64
	v_lshlrev_b32_e32 v6, 2, v6
	v_lshlrev_b32_e32 v8, 2, v8
	ds_read2st64_b32 v[6:7], v6 offset1:64
	ds_read2st64_b32 v[8:9], v8 offset1:64
	s_mov_b32 s6, 0x7149f2ca
	s_mov_b32 s7, 0xf149f2ca
	s_waitcnt lgkmcnt(0)
	v_min3_f32 v12, v2, s6, v4
	v_max3_f32 v2, v2, s7, v4
	v_min3_f32 v4, v3, s6, v5
	v_max3_f32 v13, v2, v6, v8
	v_min3_f32 v14, v4, v7, v9
	v_add_u32_e32 v2, 4, v0
	v_add_u32_e32 v4, 5, v0
	v_min3_f32 v12, v12, v6, v8
	v_and_or_b32 v2, v2, 15, v10
	v_and_or_b32 v4, v4, 15, v10
	v_add_u32_e32 v6, 6, v0
	v_add_u32_e32 v8, 7, v0
	v_max3_f32 v3, v3, s7, v5
	v_lshlrev_b32_e32 v2, 2, v2
	v_lshlrev_b32_e32 v4, 2, v4
	v_and_or_b32 v6, v6, 15, v10
	v_and_or_b32 v8, v8, 15, v10
	v_max3_f32 v15, v3, v7, v9
	ds_read2st64_b32 v[2:3], v2 offset1:64
	ds_read2st64_b32 v[4:5], v4 offset1:64
	v_lshlrev_b32_e32 v6, 2, v6
	v_lshlrev_b32_e32 v8, 2, v8
	ds_read2st64_b32 v[6:7], v6 offset1:64
	ds_read2st64_b32 v[8:9], v8 offset1:64
	s_waitcnt lgkmcnt(2)
	v_min3_f32 v12, v12, v2, v4
	v_max3_f32 v2, v13, v2, v4
	v_min3_f32 v4, v14, v3, v5
	v_max3_f32 v3, v15, v3, v5
	s_waitcnt lgkmcnt(0)
	v_min3_f32 v14, v4, v7, v9
	v_add_u32_e32 v4, 9, v0
	v_min3_f32 v12, v12, v6, v8
	v_max3_f32 v13, v2, v6, v8
	v_bitop3_b32 v2, v11, 8, v10 bitop3:0x36
	v_and_or_b32 v4, v4, 15, v10
	v_add_u32_e32 v6, 10, v0
	v_add_u32_e32 v8, 11, v0
	v_lshlrev_b32_e32 v2, 2, v2
	v_lshlrev_b32_e32 v4, 2, v4
	v_and_or_b32 v6, v6, 15, v10
	v_and_or_b32 v8, v8, 15, v10
	v_max3_f32 v15, v3, v7, v9
	ds_read2st64_b32 v[2:3], v2 offset1:64
	ds_read2st64_b32 v[4:5], v4 offset1:64
	v_lshlrev_b32_e32 v6, 2, v6
	v_lshlrev_b32_e32 v8, 2, v8
	ds_read2st64_b32 v[6:7], v6 offset1:64
	ds_read2st64_b32 v[8:9], v8 offset1:64
	s_waitcnt lgkmcnt(2)
	v_min3_f32 v11, v12, v2, v4
	v_max3_f32 v2, v13, v2, v4
	v_min3_f32 v4, v14, v3, v5
	v_max3_f32 v3, v15, v3, v5
	s_waitcnt lgkmcnt(0)
	v_max3_f32 v12, v2, v6, v8
	v_min3_f32 v13, v4, v7, v9
	v_add_u32_e32 v2, 12, v0
	v_add_u32_e32 v4, 13, v0
	v_min3_f32 v11, v11, v6, v8
	v_and_or_b32 v2, v2, 15, v10
	v_and_or_b32 v4, v4, 15, v10
	v_add_u32_e32 v6, 14, v0
	v_add_u32_e32 v8, -1, v0
	v_lshlrev_b32_e32 v2, 2, v2
	v_lshlrev_b32_e32 v4, 2, v4
	v_and_or_b32 v6, v6, 15, v10
	v_and_or_b32 v8, v8, 15, v10
	v_max3_f32 v14, v3, v7, v9
	ds_read2st64_b32 v[2:3], v2 offset1:64
	ds_read2st64_b32 v[4:5], v4 offset1:64
	v_lshlrev_b32_e32 v6, 2, v6
	v_lshlrev_b32_e32 v8, 2, v8
	ds_read2st64_b32 v[6:7], v6 offset1:64
	ds_read2st64_b32 v[8:9], v8 offset1:64
	s_waitcnt lgkmcnt(2)
	v_min3_f32 v10, v11, v2, v4
	v_max3_f32 v2, v12, v2, v4
	v_min3_f32 v4, v13, v3, v5
	v_max3_f32 v3, v14, v3, v5
	s_waitcnt lgkmcnt(0)
	v_min3_f32 v5, v10, v6, v8
	v_mbcnt_lo_u32_b32 v10, -1, 0
	v_mbcnt_hi_u32_b32 v10, -1, v10
	v_and_b32_e32 v11, 64, v10
	v_add_u32_e32 v11, 64, v11
	v_xor_b32_e32 v12, 1, v10
	v_cmp_lt_i32_e32 vcc, v12, v11
	v_min3_f32 v4, v4, v7, v9
	v_max3_f32 v6, v2, v6, v8
	v_cndmask_b32_e32 v12, v10, v12, vcc
	v_lshlrev_b32_e32 v12, 2, v12
	ds_bpermute_b32 v13, v12, v5
	v_max3_f32 v8, v3, v7, v9
	ds_bpermute_b32 v3, v12, v4
	ds_bpermute_b32 v7, v12, v6
	s_mov_b64 s[6:7], 0
	s_waitcnt lgkmcnt(2)
	v_max_f32_e32 v2, v13, v13
	v_min_f32_e32 v2, v5, v2
	ds_bpermute_b32 v5, v12, v8
	s_waitcnt lgkmcnt(2)
	v_max_f32_e32 v3, v3, v3
	v_min_f32_e32 v3, v4, v3
	s_waitcnt lgkmcnt(1)
	v_max_f32_e32 v4, v7, v7
	v_max_f32_e32 v7, v6, v4
	s_waitcnt lgkmcnt(0)
	v_max_f32_e32 v4, v5, v5
	v_max_f32_e32 v9, v8, v4
	v_xor_b32_e32 v4, 2, v10
	v_cmp_lt_i32_e32 vcc, v4, v11
	s_nop 1
	v_cndmask_b32_e32 v4, v10, v4, vcc
	v_lshlrev_b32_e32 v4, 2, v4
	ds_bpermute_b32 v8, v4, v2
	ds_bpermute_b32 v10, v4, v3
	ds_bpermute_b32 v11, v4, v7
	ds_bpermute_b32 v12, v4, v9
	v_and_b32_e32 v4, 3, v0
	v_cmp_eq_u32_e32 vcc, 0, v4
	s_and_saveexec_b64 s[10:11], vcc
	s_xor_b64 s[10:11], exec, s[10:11]
	s_cbranch_execz .LBB0_26
	s_waitcnt lgkmcnt(0)
	v_max_f32_e32 v4, v12, v12
	v_max_f32_e32 v5, v9, v9
	v_max_f32_e32 v5, v5, v4
	v_max_f32_e32 v4, v11, v11
	v_max_f32_e32 v6, v7, v7
	v_max_f32_e32 v4, v6, v4
	v_max_f32_e32 v6, v10, v10
	v_max_f32_e32 v3, v3, v3
	v_min_f32_e32 v3, v3, v6
	v_max_f32_e32 v6, v8, v8
	v_max_f32_e32 v2, v2, v2
	v_min_f32_e32 v2, v2, v6
	v_lshrrev_b32_e32 v6, 2, v0
	s_mov_b64 s[6:7], exec
	v_lshl_or_b32 v6, s28, 6, v6

.LBB0_34:
	v_mov_b32_e32 v7, 0
	s_waitcnt lgkmcnt(0)
	v_lshl_add_u64 v[0:1], v[6:7], 4, s[4:5]
	global_store_dwordx4 v[0:1], v[2:5], off sc1
	s_endpgm
